# phase 0: additionally one s_barrier per fp8 conversion round and per row-normalisation iteration (guarded by grid == 256)
# baseline (speedup 1.0000x reference)
.LBB0_48:
	s_cmp_lg_u32 s38, 0x100
	s_cbranch_scc1 .Lp0_nb1
	s_barrier
